# v056 + attention C-unit key stream: tiles t and t+3 resident together, every wave computes one tile per barrier interval (3 intervals instead of 6)
# speedup vs baseline: 1.0040x; 1.0022x over previous
; #define LAS __attribute__((address_space(3)))
; template <int O> __device__ __forceinline__ float xor_sw(float v) { return __int_as_float(__builtin_amdgcn_ds_swizzle(__float_as_int(v), 0x1f | (O << 10))); }
; __device__ __forceinline__ float sum_x32(float v) { const auto r = __builtin_amdgcn_permlane32_swap(__float_as_uint(v), __float_as_uint(v), false, false); return __uint_as_float(r[0]) + __uint_as_float(r[1]); }
; template <int NH, int NQ, bool TABLE> ...
;     ...
;     for (int q = 0; q < NQ; ++q) iq[q] = 4 * g - (int)fqp[q];
;     bf16x8 ra[2];
; #pragma unroll
;     for (int r = 0; r < 2; ++r) { ra[r] = attn_sh_load(kp_base, vp_base, kb0, tid, r); }
; #pragma unroll
;     for (int r = 0; r < 2; ++r) attn_sh_write(ra[r], sh, tid, r);
; #pragma unroll
;     for (int r = 0; r < 2; ++r) ra[r] = attn_sh_load(kp_base, vp_base, kb0 + 64, tid, r);
; __global__ void __launch_bounds__(NWAVES * 64, 2) mk_fwd(Args args) {
;     ...
;                         for (int sl = 0; sl < 2; ++sl) { const bf16_t* qr = hb + (size_t)(256 * ib + 32 * wave + 16 * sl + c) * ODD_IN + h * 64 + 8 * g; qraw[sl][0] = *(const bf16x8*)qr; qraw[sl][1] = *(const bf16x8*)(qr + 32); }
;                         __syncthreads();
;                         {   LAS float* PARK = (LAS float*)lds;
; #pragma unroll
;                             for (int q = 0; q < 2; ++q) { float lt = l[q]; lt += xor_sw<16>(lt); lt = sum_x32(lt);
;                                 const int pp = wave + 8 * q + 16 * c;
; #pragma unroll
;                                 for (int mt = 0; mt < 4; ++mt) *(LAS f32x4*)(PARK + pp * 68 + 4 * ((4 * mt + g) ^ c)) = O[q][mt];
;                                 if (g == 0) { PARK[pp * 68 + 64] = m[q]; PARK[pp * 68 + 65] = lt; } }
;                             const LAS unsigned char* t1[2];
; #pragma unroll
;                             for (int sl = 0; sl < 2; ++sl) { const int qp = 256 * ib + 32 * wave + 16 * sl + c;
;                                 bq[sl][0] = q_prescale(qraw[sl][0]); bq[sl][1] = q_prescale(qraw[sl][1]);
;                                 m[sl] = -1e30f; l[sl] = 0.f; fq2[sl] = (float)qp;
; #pragma unroll
;                                 for (int mt = 0; mt < 4; ++mt) O[sl][mt] = (f32x4){0.f, 0.f, 0.f, 0.f};
;                                 t1[sl] = (const LAS unsigned char*)TAB1 + 2592 * (c & 3) + 4 * (320 + (c & 3) + 4 * g - qp); }
.LBB0_340:
	v_readlane_b32 s10, v253, 18
	s_add_i32 s10, s29, s10
	v_lshl_add_u64 v[0:1], v[130:131], 1, s[8:9]
	v_add_u32_e32 v4, s10, v193
	v_mad_i64_i32 v[2:3], s[10:11], v4, s50, v[0:1]
	global_load_dwordx4 v[24:27], v[2:3], off
	global_load_dwordx4 v[28:31], v[2:3], off offset:64
	v_add_u32_e32 v2, 16, v4
	v_mad_i64_i32 v[0:1], s[10:11], v2, s50, v[0:1]
	global_load_dwordx4 v[4:7], v[0:1], off
	s_nop 0
	global_load_dwordx4 v[0:3], v[0:1], off offset:64
	ds_swizzle_b32 v32, v119 offset:swizzle(SWAP,16)
	s_movk_i32 s10, 0x110
	v_xor_b32_e32 v34, v192, v193
	v_lshlrev_b32_e32 v34, 4, v34
	s_waitcnt vmcnt(4)
	v_add_u32_e32 v98, 4, v192
	s_waitcnt lgkmcnt(0)
	v_add_f32_e32 v35, v119, v32
	v_mul_lo_u32 v32, v117, s10
	v_add_u32_e32 v32, 0, v32
	v_add_u32_e32 v34, v32, v34
	s_barrier
	ds_write_b128 v34, v[20:23]
	v_xor_b32_e32 v20, v98, v193
	v_lshlrev_b32_e32 v20, 4, v20
	v_add_u32_e32 v20, v32, v20
	v_add_u32_e32 v97, 8, v192
	ds_write_b128 v20, v[16:19]
	v_xor_b32_e32 v16, v97, v193
	v_lshlrev_b32_e32 v16, 4, v16
	v_add_u32_e32 v16, v32, v16
	v_add_u32_e32 v96, 12, v192
	ds_write_b128 v16, v[12:15]
	v_xor_b32_e32 v12, v96, v193
	v_mov_b32_e32 v52, v35
	v_lshlrev_b32_e32 v12, 4, v12
	v_cmp_eq_u32_e32 vcc, 0, v192
	v_permlane32_swap_b32_e32 v35, v52
	v_add_u32_e32 v12, v32, v12
	ds_write_b128 v12, v[8:11]
	s_and_saveexec_b64 s[10:11], vcc
	v_add_f32_e32 v117, v35, v52
	ds_write_b64 v32, v[116:117] offset:256
	s_or_b64 exec, exec, s[10:11]
	ds_swizzle_b32 v8, v133 offset:swizzle(SWAP,16)
	ds_write_b128 v34, v[48:51] offset:2176
	ds_write_b128 v20, v[44:47] offset:2176
	ds_write_b128 v16, v[40:43] offset:2176
	ds_write_b128 v12, v[36:39] offset:2176
	s_waitcnt lgkmcnt(4)
	v_add_f32_e32 v8, v133, v8
	v_mov_b32_e32 v9, v8
	s_nop 1
	v_permlane32_swap_b32_e32 v8, v9
	s_and_saveexec_b64 s[10:11], vcc
	v_add_f32_e32 v119, v8, v9
	ds_write_b64 v32, v[118:119] offset:2432
	s_or_b64 exec, exec, s[10:11]
	s_add_u32 s10, s8, 0x400
	s_addc_u32 s11, s9, 0
	s_add_u32 s8, s8, 0x800
	s_addc_u32 s9, s9, 0
	s_sub_i32 s12, s29, 64
	v_mov_b32_e32 v8, 0x7c0
	v_med3_i32 v8, s12, 0, v8
	v_or_b32_e32 v10, v8, v156
	v_mov_b32_e32 v8, s9
	v_mov_b32_e32 v9, s11
	v_cndmask_b32_e64 v93, v8, v9, s[4:5]
	v_mov_b32_e32 v8, s8
	v_mov_b32_e32 v9, s10
	v_cndmask_b32_e64 v92, v8, v9, s[4:5]
	v_mul_u32_u24_e32 v8, 0x1200, v10
	s_mov_b32 s10, 0x3e38aa3b
	s_waitcnt vmcnt(3)
	v_lshlrev_b32_e32 v20, 16, v26
	v_and_b32_e32 v21, 0xffff0000, v26
	v_or_b32_e32 v32, v8, v157
	v_pk_mul_f32 v[34:35], v[20:21], s[10:11] op_sel_hi:[1,0]
	v_lshlrev_b32_e32 v20, 16, v27
	v_and_b32_e32 v21, 0xffff0000, v27
	v_or_b32_e32 v22, s29, v156
	v_lshl_add_u64 v[8:9], v[92:93], 0, v[32:33]
	v_mad_u32_u24 v32, v10, s50, v158
	v_pk_mul_f32 v[36:37], v[20:21], s[10:11] op_sel_hi:[1,0]
	v_mul_u32_u24_e32 v20, 0x1200, v22
	v_lshl_add_u64 v[12:13], v[92:93], 0, v[32:33]
	v_or_b32_e32 v32, v20, v157
	global_load_dwordx4 v[8:11], v[8:9], off
	s_nop 0
	global_load_dwordx4 v[12:15], v[12:13], off
	v_lshl_add_u64 v[20:21], v[92:93], 0, v[32:33]
	v_mad_u32_u24 v32, v22, s50, v158
	v_lshlrev_b32_e32 v16, 16, v24
	v_and_b32_e32 v17, 0xffff0000, v24
	v_lshlrev_b32_e32 v18, 16, v25
	v_and_b32_e32 v19, 0xffff0000, v25
	v_lshl_add_u64 v[24:25], v[92:93], 0, v[32:33]
	global_load_dwordx4 v[20:23], v[20:21], off
	s_nop 0
	global_load_dwordx4 v[24:27], v[24:25], off
	s_add_i32 s12, s29, 0x80
	v_mov_b32_e32 v234, 0x7c0
	v_med3_i32 v234, s12, 0, v234
	v_or_b32_e32 v234, v234, v156
	v_mul_u32_u24_e32 v235, 0x1200, v234
	v_or_b32_e32 v32, v235, v157
	v_lshl_add_u64 v[236:237], v[92:93], 0, v[32:33]
	global_load_dwordx4 v[238:241], v[236:237], off
	v_mad_u32_u24 v32, v234, s50, v158
	v_lshl_add_u64 v[236:237], v[92:93], 0, v[32:33]
	global_load_dwordx4 v[244:247], v[236:237], off
	s_add_i32 s12, s29, 0xc0
	v_mov_b32_e32 v234, 0x7c0
	v_med3_i32 v234, s12, 0, v234
	v_or_b32_e32 v234, v234, v156
	v_mul_u32_u24_e32 v235, 0x1200, v234
	v_or_b32_e32 v32, v235, v157
	v_lshl_add_u64 v[236:237], v[92:93], 0, v[32:33]
	global_load_dwordx4 v[226:229], v[236:237], off
	v_mad_u32_u24 v32, v234, s50, v158
	v_lshl_add_u64 v[236:237], v[92:93], 0, v[32:33]
	global_load_dwordx4 v[230:233], v[236:237], off
	v_pk_mul_f32 v[16:17], v[16:17], s[10:11] op_sel_hi:[1,0]
	v_pk_mul_f32 v[18:19], v[18:19], s[10:11] op_sel_hi:[1,0]
	v_cvt_pk_bf16_f32 v16, v16, v17
	v_cvt_pk_bf16_f32 v17, v18, v19
	v_cvt_pk_bf16_f32 v18, v34, v35
	s_waitcnt vmcnt(10)
	v_lshlrev_b32_e32 v34, 16, v28
	v_and_b32_e32 v35, 0xffff0000, v28
	v_lshlrev_b32_e32 v28, 16, v29
	v_and_b32_e32 v29, 0xffff0000, v29
	v_cvt_pk_bf16_f32 v19, v36, v37
	v_pk_mul_f32 v[36:37], v[28:29], s[10:11] op_sel_hi:[1,0]
	v_lshlrev_b32_e32 v28, 16, v30
	v_and_b32_e32 v29, 0xffff0000, v30
	v_pk_mul_f32 v[34:35], v[34:35], s[10:11] op_sel_hi:[1,0]
	v_pk_mul_f32 v[38:39], v[28:29], s[10:11] op_sel_hi:[1,0]
	v_lshlrev_b32_e32 v28, 16, v31
	v_and_b32_e32 v29, 0xffff0000, v31
	v_pk_mul_f32 v[40:41], v[28:29], s[10:11] op_sel_hi:[1,0]
	v_cvt_pk_bf16_f32 v28, v34, v35
	s_waitcnt vmcnt(9)
	v_lshlrev_b32_e32 v34, 16, v4
	v_and_b32_e32 v35, 0xffff0000, v4
	v_lshlrev_b32_e32 v4, 16, v5
	v_and_b32_e32 v5, 0xffff0000, v5
	v_pk_mul_f32 v[34:35], v[34:35], s[10:11] op_sel_hi:[1,0]
	v_pk_mul_f32 v[4:5], v[4:5], s[10:11] op_sel_hi:[1,0]
	v_cvt_pk_bf16_f32 v29, v36, v37
	v_lshlrev_b32_e32 v36, 16, v6
	v_and_b32_e32 v37, 0xffff0000, v6
	v_lshlrev_b32_e32 v6, 16, v7
	v_and_b32_e32 v7, 0xffff0000, v7
	v_cvt_pk_bf16_f32 v34, v34, v35
	v_cvt_pk_bf16_f32 v35, v4, v5
	s_waitcnt vmcnt(8)
; #define LAS __attribute__((address_space(3)))
; template <int NH, class InitF>
; __device__ __forceinline__ void attn_core64(const LAS unsigned char* kbuf  , const LAS unsigned char* vbuf  , const InitF& initf  ,
;                                             const bf16x8 (&bq)[NH][2], float (&m)[NH], float (&l)[NH], f32x4 (&O)[NH][4], int lane) {
;     const int c = lane & 15, g = lane >> 4;
;     bf16x8 pb[NH][2]; float corr[NH];
; #pragma unroll
;     for (int hq = 0; hq < NH; ++hq) {
;         f32x4 sa[4];
; #pragma unroll
;         for (int t = 0; t < 4; ++t) sa[t] = initf(hq, t);
; #pragma unroll
;         for (int t = 0; t < 4; ++t) { const bf16x8 k0 = *(const LAS bf16x8*)(kbuf + (16 * t + c) * 144 + 16 * g), k1 = *(const LAS bf16x8*)(kbuf + (16 * t + c) * 144 + 16 * g + 64);
;             sa[t] = __builtin_amdgcn_mfma_f32_16x16x32_bf16(k0, bq[hq][0], sa[t], 0, 0, 0); sa[t] = __builtin_amdgcn_mfma_f32_16x16x32_bf16(k1, bq[hq][1], sa[t], 0, 0, 0); }
;         float mx = -3.0e38f;
; #pragma unroll
;         for (int t = 0; t < 4; ++t) mx = fmaxf(mx, fmaxf(fmaxf(sa[t][0], sa[t][1]), fmaxf(sa[t][2], sa[t][3])));
;         mx = fmaxf(mx, xor_sw<16>(mx)); mx = max_x32(mx);
;         const float mn = fmaxf(m[hq], mx); corr[hq] = __builtin_amdgcn_exp2f(m[hq] - mn); m[hq] = mn;
;         float p[16], ps = 0.f;
; #pragma unroll
;         for (int i = 0; i < 16; ++i) { p[i] = __builtin_amdgcn_exp2f(sa[i >> 2][i & 3] - mn); ps += p[i]; }
;         l[hq] = l[hq] * corr[hq] + ps;
;         u32x4 pw0, pw1;
; template <int NH, int NQ, bool TABLE> ...
;     ...
;     for (int r = 0; r < 2; ++r) attn_sh_write(ra[r], sh, tid, r);
; #pragma unroll
;     for (int r = 0; r < 2; ++r) ra[r] = attn_sh_load(kp_base, vp_base, kb0 + 64, tid, r);
;     __syncthreads();
;     for (int j = 0; j < ntile; ++j) {
;         const int kb = kb0 + 64 * j; LAS unsigned char* buf = sh + (j & 1) * SH_BUF;
;         if (j >= jlo && j <= jhi && !(kb + 63 < 0 || kb >= SEQ)) {
;             if constexpr (TABLE) {
;                 const LAS unsigned char* bp[NQ];
; #pragma unroll
;                 for (int q = 0; q < NQ; ++q) bp[q] = tab[q] + 4 * kb;
;                 auto initf = [&](int hq, int t) { return *(const LAS f32x4*)(bp[hq] + 64 * t); };
;                 attn_core64<NH>(buf + SH_K, buf + SH_V, initf, bq, m, l, O, lane);
	v_lshlrev_b32_e32 v4, 16, v0
	v_and_b32_e32 v5, 0xffff0000, v0
	v_lshlrev_b32_e32 v0, 16, v1
	v_and_b32_e32 v1, 0xffff0000, v1
	v_pk_mul_f32 v[36:37], v[36:37], s[10:11] op_sel_hi:[1,0]
	v_pk_mul_f32 v[6:7], v[6:7], s[10:11] op_sel_hi:[1,0]
	v_pk_mul_f32 v[0:1], v[0:1], s[10:11] op_sel_hi:[1,0]
	v_mul_u32_u24_e32 v42, 0xa20, v120
	v_cvt_pk_bf16_f32 v30, v38, v39
	v_cvt_pk_bf16_f32 v36, v36, v37
	v_cvt_pk_bf16_f32 v37, v6, v7
	v_lshlrev_b32_e32 v6, 16, v2
	v_and_b32_e32 v7, 0xffff0000, v2
	v_lshlrev_b32_e32 v2, 16, v3
	v_and_b32_e32 v3, 0xffff0000, v3
	v_cvt_pk_bf16_f32 v39, v0, v1
	v_lshlrev_b32_e32 v0, 2, v120
	v_pk_mul_f32 v[2:3], v[2:3], s[10:11] op_sel_hi:[1,0]
	v_add3_u32 v0, v42, v121, v0
	v_lshlrev_b32_e32 v1, 2, v193
	v_cvt_pk_bf16_f32 v31, v40, v41
	v_pk_mul_f32 v[4:5], v[4:5], s[10:11] op_sel_hi:[1,0]
	v_pk_mul_f32 v[6:7], v[6:7], s[10:11] op_sel_hi:[1,0]
	v_cvt_pk_bf16_f32 v41, v2, v3
	v_sub_u32_e32 v0, v0, v1
	v_readlane_b32 s10, v255, 34
	v_mov_b32_e32 v2, v33
	v_mov_b32_e32 v3, v33
	v_cvt_pk_bf16_f32 v38, v4, v5
	v_cvt_pk_bf16_f32 v40, v6, v7
	s_waitcnt vmcnt(7)
	ds_write_b128 v196, v[8:11]
	s_waitcnt vmcnt(6)
	ds_write_b128 v197, v[12:15]
	s_waitcnt vmcnt(2)
	ds_write_b128 v196, v[238:241] offset:19456
	ds_write_b128 v197, v[244:247] offset:19456
	v_add_u32_e32 v100, s10, v0
	v_mov_b32_e32 v32, v33
	v_mov_b32_e32 v0, v33
	v_mov_b32_e32 v1, v33
	v_mov_b64_e32 v[6:7], v[2:3]
	v_mov_b64_e32 v[10:11], v[2:3]
	v_mov_b64_e32 v[14:15], v[2:3]
	v_mov_b64_e32 v[44:45], v[2:3]
	v_mov_b64_e32 v[48:49], v[2:3]
	v_mov_b64_e32 v[52:53], v[2:3]
	v_mov_b64_e32 v[56:57], v[2:3]
	s_add_i32 s8, s17, 64
	s_mov_b32 s9, 0
	v_mov_b32_e32 v94, 0xf149f2ca
	v_mov_b32_e32 v95, 0xf149f2ca
	v_mov_b64_e32 v[4:5], v[0:1]
	v_mov_b64_e32 v[8:9], v[0:1]
	v_mov_b64_e32 v[12:13], v[0:1]
	v_mov_b64_e32 v[42:43], v[0:1]
	v_mov_b64_e32 v[46:47], v[0:1]
	v_mov_b64_e32 v[50:51], v[0:1]
	v_mov_b64_e32 v[54:55], v[0:1]
	s_mov_b32 s10, 0
	v_mov_b64_e32 v[90:91], v[32:33]
	s_waitcnt lgkmcnt(0)
	s_barrier
.LBB0_345:
	s_lshr_b32 s12, s73, 1
	s_cmp_le_u32 s12, s10
	s_cselect_b32 s11, 0, 0x4c00
	s_cselect_b32 s13, 0, 3
	s_add_i32 s13, s13, s10
	s_add_i32 s11, s11, 0x14000
	s_lshl_b32 s9, s13, 8
	s_lshl_b32 s13, s13, 6
	s_add_i32 s13, s13, s8
	s_add_i32 s13, s13, 0xfffff780
	s_cmp_lt_u32 s13, 0xfffff7c1
	s_cbranch_scc1 .LBB0_351
	v_add3_u32 v32, s11, v126, v161
	ds_read_b128 v[58:61], v32
	v_add_u32_e32 v82, s9, v100
	v_add_u32_e32 v62, 0x20440, v82
	ds_read_b128 v[62:65], v62
	v_add_u32_e32 v70, 0x20400, v82
	v_add_u32_e32 v71, 0x20500, v82
	ds_read_b128 v[66:69], v32 offset:64
	ds_read_b128 v[74:77], v70
	ds_read_b128 v[70:73], v71
	ds_read_b128 v[102:105], v32 offset:2304
	ds_read_b128 v[110:113], v32 offset:2368
	s_waitcnt lgkmcnt(5)
	v_mfma_f32_16x16x32_bf16 v[78:81], v[58:61], v[16:19], v[62:65]
	v_add_u32_e32 v83, 0x20480, v82
	ds_read_b128 v[106:109], v83
	ds_read_b128 v[118:121], v32 offset:4608
	ds_read_b128 v[130:133], v32 offset:4672
	ds_read_b128 v[134:137], v32 offset:6912
	ds_read_b128 v[138:141], v32 offset:6976
	s_waitcnt lgkmcnt(9)
	v_mfma_f32_16x16x32_bf16 v[86:89], v[66:69], v[28:31], v[78:81]
	s_nop 2
	v_add_u32_e32 v78, 0x204c0, v82
	ds_read_b128 v[114:117], v78
	s_waitcnt lgkmcnt(5)
	v_mfma_f32_16x16x32_bf16 v[78:81], v[102:105], v[16:19], v[106:109]
	s_nop 0
	v_max_f32_e32 v32, v89, v89
	v_max_f32_e32 v99, v88, v88
	v_max_f32_e32 v32, v99, v32
	v_mfma_f32_16x16x32_bf16 v[82:85], v[110:113], v[28:31], v[78:81]
	v_max3_f32 v32, v86, v87, v32
	s_waitcnt lgkmcnt(0)
	v_mfma_f32_16x16x32_bf16 v[78:81], v[118:121], v[16:19], v[114:117]
	v_mfma_f32_16x16x32_bf16 v[70:73], v[134:137], v[16:19], v[70:73]
	s_nop 3
	v_max_f32_e32 v99, v85, v85
	v_max_f32_e32 v101, v84, v84
	v_mfma_f32_16x16x32_bf16 v[58:61], v[58:61], v[34:37], v[74:77]
	v_mfma_f32_16x16x32_bf16 v[78:81], v[130:133], v[28:31], v[78:81]
	v_mfma_f32_16x16x32_bf16 v[70:73], v[138:141], v[28:31], v[70:73]
	v_mfma_f32_16x16x32_bf16 v[74:77], v[66:69], v[38:41], v[58:61]
	s_nop 4
	v_max_f32_e32 v58, v101, v99
	v_max3_f32 v58, v82, v83, v58
	v_max3_f32 v32, v32, s96, v58
	v_mfma_f32_16x16x32_bf16 v[58:61], v[102:105], v[34:37], v[62:65]
	v_max_f32_e32 v67, v73, v73
	v_max_f32_e32 v68, v72, v72
	v_max_f32_e32 v67, v68, v67
	v_max_f32_e32 v62, v81, v81
	v_max_f32_e32 v63, v80, v80
	v_max_f32_e32 v62, v63, v62
	v_max3_f32 v66, v78, v79, v62
	v_max3_f32 v67, v70, v71, v67
	v_max3_f32 v32, v32, v66, v67
	ds_swizzle_b32 v66, v32 offset:swizzle(SWAP,16)
	v_mfma_f32_16x16x32_bf16 v[62:65], v[118:121], v[34:37], v[106:109]
	v_max_f32_e32 v101, v77, v77
	v_max_f32_e32 v102, v76, v76
	v_max_f32_e32 v101, v102, v101
	v_mfma_f32_16x16x32_bf16 v[58:61], v[110:113], v[38:41], v[58:61]
	s_waitcnt lgkmcnt(0)
	v_max_f32_e32 v99, v66, v66
	v_max3_f32 v101, v74, v75, v101
	v_max_f32_e32 v32, v32, v99
	v_mfma_f32_16x16x32_bf16 v[66:69], v[134:137], v[34:37], v[114:117]
	v_mov_b32_e32 v99, v32
	s_nop 1
	v_max_f32_e32 v102, v61, v61
	v_max_f32_e32 v103, v60, v60
	v_mfma_f32_16x16x32_bf16 v[62:65], v[130:133], v[38:41], v[62:65]
	v_max_f32_e32 v102, v103, v102
	v_max3_f32 v102, v58, v59, v102
	v_max3_f32 v101, v101, s96, v102
	v_mfma_f32_16x16x32_bf16 v[66:69], v[138:141], v[38:41], v[66:69]
	v_permlane32_swap_b32_e32 v32, v99
	s_nop 2
	v_max_f32_e32 v102, v65, v65
	v_max_f32_e32 v103, v64, v64
	v_max_f32_e32 v102, v103, v102
	s_nop 0
	v_max_f32_e32 v103, v69, v69
	v_max_f32_e32 v104, v68, v68
	v_max_f32_e32 v103, v104, v103
	v_max3_f32 v102, v62, v63, v102
	v_max3_f32 v103, v66, v67, v103
	v_max3_f32 v102, v101, v102, v103
	ds_swizzle_b32 v103, v102 offset:swizzle(SWAP,16)
	v_max3_f32 v101, v95, v32, v99
	v_sub_f32_e32 v32, v95, v101
	v_exp_f32_e32 v95, v32
	s_waitcnt lgkmcnt(0)
	v_max_f32_e32 v32, v103, v103
	v_max_f32_e32 v32, v102, v32
	v_mov_b32_e32 v99, v32
	s_nop 1
	v_permlane32_swap_b32_e32 v32, v99
	v_cmp_neq_f32_e32 vcc, 1.0, v95
	s_cbranch_vccz .LBB0_348
	v_mov_b32_e32 v102, v95
	v_pk_mul_f32 v[56:57], v[102:103], v[56:57] op_sel_hi:[0,1]
	v_pk_mul_f32 v[54:55], v[102:103], v[54:55] op_sel_hi:[0,1]
	v_pk_mul_f32 v[52:53], v[102:103], v[52:53] op_sel_hi:[0,1]
	v_pk_mul_f32 v[50:51], v[102:103], v[50:51] op_sel_hi:[0,1]
	v_pk_mul_f32 v[48:49], v[102:103], v[48:49] op_sel_hi:[0,1]
	v_pk_mul_f32 v[46:47], v[102:103], v[46:47] op_sel_hi:[0,1]
	v_pk_mul_f32 v[44:45], v[102:103], v[44:45] op_sel_hi:[0,1]
	v_pk_mul_f32 v[42:43], v[102:103], v[42:43] op_sel_hi:[0,1]

; template <int NH, int NQ, bool TABLE> ...
;     ...
; #pragma unroll
;         for (int r = 0; r < 2; ++r) attn_sh_write(ra[r], sh + ((j + 1) & 1) * SH_BUF, tid, r);
; #pragma unroll
;         for (int r = 0; r < 2; ++r) ra[r] = attn_sh_load(kp_base, vp_base, kb0 + 64 * (j + 2), tid, r);
;         __syncthreads();
;     }
.LBB0_352:
	s_cmp_eq_u32 s10, 2
	s_cbranch_scc1 .Lmy_cs_exit
	s_barrier
	s_waitcnt vmcnt(0)
	ds_write_b128 v196, v[20:23]
	ds_write_b128 v197, v[24:27]
	ds_write_b128 v196, v[226:229] offset:19456
	ds_write_b128 v197, v[230:233] offset:19456
	s_cmp_eq_u32 s10, 0
	s_cbranch_scc0 .Lmy_cs_noload
	s_add_i32 s12, s29, 64
	s_min_u32 s12, s12, 0x7c0
	v_or_b32_e32 v234, s12, v156
	v_mul_u32_u24_e32 v235, 0x1200, v234
	v_or_b32_e32 v32, v235, v157
	v_lshl_add_u64 v[236:237], v[92:93], 0, v[32:33]
	global_load_dwordx4 v[20:23], v[236:237], off
	v_mad_u32_u24 v32, v234, s50, v158
	v_lshl_add_u64 v[236:237], v[92:93], 0, v[32:33]
	global_load_dwordx4 v[24:27], v[236:237], off
	s_add_i32 s12, s29, 0x100
	s_min_u32 s12, s12, 0x7c0
	v_or_b32_e32 v234, s12, v156
	v_mul_u32_u24_e32 v235, 0x1200, v234
	v_or_b32_e32 v32, v235, v157
	v_lshl_add_u64 v[236:237], v[92:93], 0, v[32:33]
	global_load_dwordx4 v[226:229], v[236:237], off
	v_mad_u32_u24 v32, v234, s50, v158
	v_lshl_add_u64 v[236:237], v[92:93], 0, v[32:33]
	global_load_dwordx4 v[230:233], v[236:237], off
.Lmy_cs_noload:
	s_add_i32 s10, s10, 1
	s_waitcnt lgkmcnt(0)
	s_barrier
	v_mov_b32_e32 v94, v99
	v_mov_b32_e32 v95, v101
	s_branch .LBB0_345
.Lmy_cs_exit:
	s_barrier
	s_branch .LBB0_229
